# rope epilogue: cos/sin table loads issued lane-transposed (quad = 64 contiguous bytes of a row) and returned to accumulator layout with ds_bpermute
# speedup vs baseline: 1.0051x; 1.0051x over previous
; #define PG8_ST8(rs, b0, p, v) __builtin_amdgcn_raw_buffer_store_b64(v, rs, (int)((const char*)(p) - (const char*)(b0)), 0, 16)
; __device__ __forceinline__ unsigned cvt_pk_bf16(float lo, float hi) { unsigned r; asm volatile("v_cvt_pk_bf16_f32 %0, %1, %2" : "=v"(r) : "v"(lo), "v"(hi)); return r; }
;     __device__ __forceinline__ void operator()(const f32x4 (&acc)[2][2][4][2], const Unit& u, int wr, int wc, int fr, int fq) const {
;     ...
;             const float sc = (pn <= 6 || (pn >= 9 && pn <= 11)) ? qscale : 1.0f;
;             const int f = 16 * (wc & 1) + 4 * fq, col0 = pn * BM + 64 * (wc >> 1) + f;
; #pragma unroll
;             for (int ai = 0; ai < 2; ++ai) {
;                 f32x4 c4[4], s4[4];
; #pragma unroll
;                 for (int m = 0; m < 4; ++m) { const int row = row0 + ai * HALF + m * 16; c4[m] = *(const f32x4*)(rc + (size_t)row * 32 + f); s4[m] = *(const f32x4*)(rs + (size_t)row * 32 + f); }
;                 asm volatile("" ::: "memory");
; #pragma unroll
;                 for (int m = 0; m < 4; ++m) { const int row = row0 + ai * HALF + m * 16;
;                     const f32x4 cc = c4[m] * sc, ss = s4[m] * sc;
;                     bf16_t* rowp = P + (size_t)row * ldp + col0;
; #pragma unroll
;                     for (int bj = 0; bj < 2; ++bj) { const f32x4 x1 = acc[ai][bj][m][0], x2 = acc[ai][bj][m][1]; const f32x4 o1 = x1 * cc - x2 * ss, o2 = x2 * cc + x1 * ss;
;                         u32x2 w1, w2; w1.x = cvt_pk_bf16(o1[0], o1[1]); w1.y = cvt_pk_bf16(o1[2], o1[3]); w2.x = cvt_pk_bf16(o2[0], o2[1]); w2.y = cvt_pk_bf16(o2[2], o2[3]);
;                         PG8_ST8(rsp_, P, rowp + bj * HALF, w1); PG8_ST8(rsp_, P, rowp + bj * HALF + 32, w2); } }
.LBB0_230:
	v_lshl_add_u32 v164, s27, 8, v175
	s_add_i32 s27, s62, s56
	s_cmp_gt_i32 s27, 3
	s_mov_b64 s[34:35], -1
	s_cbranch_scc0 .LBB0_237
	s_cmp_lg_u32 s27, 8
	s_cselect_b64 s[34:35], -1, 0
	s_cmp_lt_u32 s27, 15
	s_cselect_b64 s[36:37], -1, 0
	s_and_b64 s[36:37], s[34:35], s[36:37]
	s_mov_b64 s[34:35], -1
	s_and_b64 vcc, exec, s[36:37]
	v_add_u32_e32 v172, 0x80, v164
	v_add_u32_e32 v170, 0x90, v164
	v_add_u32_e32 v168, 0xa0, v164
	v_add_u32_e32 v166, 0xb0, v164
	s_cbranch_vccz .LBB0_233
	v_lshrrev_b32_e32 v252, 2, v215
	v_and_b32_e32 v245, 15, v215
	v_sub_u32_e32 v252, v252, v245
	v_lshlrev_b32_e32 v245, 4, v245
	v_lshrrev_b32_e32 v246, 4, v215
	v_lshl_or_b32 v245, v246, 2, v245
	v_and_b32_e32 v248, 3, v215
	v_sub_u32_e32 v246, v248, v246
	v_lshlrev_b32_e32 v252, 7, v252
	v_lshl_add_u32 v248, v246, 4, v252
	v_ashrrev_i32_e32 v249, 31, v248
	v_lshl_add_u64 v[246:247], v[154:155], 0, v[248:249]
	v_lshl_add_u64 v[248:249], v[156:157], 0, v[248:249]
	s_cmp_lt_u32 s27, 7
	s_cselect_b64 s[34:35], -1, 0
	s_add_i32 s36, s27, -9
	s_cmp_lt_u32 s36, 3
	s_cselect_b64 s[36:37], -1, 0
	s_or_b64 vcc, s[34:35], s[36:37]
	v_mov_b32_e32 v132, 0x3e38aa3b
	v_ashrrev_i32_e32 v165, 31, v164
	v_cndmask_b32_e32 v174, 1.0, v132, vcc
	v_lshlrev_b64 v[132:133], 7, v[164:165]
	v_lshl_add_u64 v[134:135], v[246:247], 0, v[132:133]
	v_lshl_add_u64 v[132:133], v[248:249], 0, v[132:133]
	global_load_dwordx4 v[176:179], v[134:135], off
	global_load_dwordx4 v[184:187], v[132:133], off
	v_or_b32_e32 v192, 16, v164
	v_ashrrev_i32_e32 v193, 31, v192
	v_lshlrev_b64 v[132:133], 7, v[192:193]
	v_lshl_add_u64 v[134:135], v[246:247], 0, v[132:133]
	v_lshl_add_u64 v[132:133], v[248:249], 0, v[132:133]
	global_load_dwordx4 v[188:191], v[134:135], off
	global_load_dwordx4 v[218:221], v[132:133], off
	v_or_b32_e32 v182, 32, v164
	v_ashrrev_i32_e32 v183, 31, v182
	v_lshlrev_b64 v[132:133], 7, v[182:183]
	v_lshl_add_u64 v[134:135], v[246:247], 0, v[132:133]
	v_lshl_add_u64 v[132:133], v[248:249], 0, v[132:133]
	global_load_dwordx4 v[144:147], v[134:135], off
	global_load_dwordx4 v[140:143], v[132:133], off
	v_or_b32_e32 v180, 48, v164
	v_ashrrev_i32_e32 v181, 31, v180
	v_lshlrev_b64 v[132:133], 7, v[180:181]
	v_lshl_add_u64 v[134:135], v[246:247], 0, v[132:133]
	v_lshl_add_u64 v[132:133], v[248:249], 0, v[132:133]
	global_load_dwordx4 v[136:139], v[134:135], off
	s_movk_i32 s36, 0x2400
	global_load_dwordx4 v[132:135], v[132:133], off
	v_ashrrev_i32_e32 v173, 31, v172
	v_ashrrev_i32_e32 v171, 31, v170
	v_ashrrev_i32_e32 v169, 31, v168
	v_ashrrev_i32_e32 v167, 31, v166
	s_waitcnt vmcnt(0)
	ds_bpermute_b32 v176, v245, v176
	ds_bpermute_b32 v177, v245, v177
	ds_bpermute_b32 v178, v245, v178
	ds_bpermute_b32 v179, v245, v179
	ds_bpermute_b32 v184, v245, v184
	ds_bpermute_b32 v185, v245, v185
	ds_bpermute_b32 v186, v245, v186
	ds_bpermute_b32 v187, v245, v187
	ds_bpermute_b32 v188, v245, v188
	ds_bpermute_b32 v189, v245, v189
	ds_bpermute_b32 v190, v245, v190
	ds_bpermute_b32 v191, v245, v191
	ds_bpermute_b32 v218, v245, v218
	ds_bpermute_b32 v219, v245, v219
	ds_bpermute_b32 v220, v245, v220
	ds_bpermute_b32 v221, v245, v221
	ds_bpermute_b32 v144, v245, v144
	ds_bpermute_b32 v145, v245, v145
	ds_bpermute_b32 v146, v245, v146
	ds_bpermute_b32 v147, v245, v147
	ds_bpermute_b32 v140, v245, v140
	ds_bpermute_b32 v141, v245, v141
	ds_bpermute_b32 v142, v245, v142
	ds_bpermute_b32 v143, v245, v143
	ds_bpermute_b32 v136, v245, v136
	ds_bpermute_b32 v137, v245, v137
	ds_bpermute_b32 v138, v245, v138
	ds_bpermute_b32 v139, v245, v139
	ds_bpermute_b32 v132, v245, v132
	ds_bpermute_b32 v133, v245, v133
	ds_bpermute_b32 v134, v245, v134
	ds_bpermute_b32 v135, v245, v135
	s_waitcnt lgkmcnt(0)
	v_pk_mul_f32 v[198:199], v[174:175], v[178:179] op_sel_hi:[0,1]
	v_pk_mul_f32 v[186:187], v[174:175], v[186:187] op_sel_hi:[0,1]
	v_pk_mul_f32 v[184:185], v[174:175], v[184:185] op_sel_hi:[0,1]
	v_pk_mul_f32 v[200:201], v[174:175], v[176:177] op_sel_hi:[0,1]
	v_mov_b64_e32 v[176:177], s[20:21]
	v_lshrrev_b32_e32 v252, 2, v215
	v_and_b32_e32 v228, 15, v215
	v_sub_u32_e32 v252, v252, v228
	v_mad_i64_i32 v[176:177], s[34:35], v252, s36, v[176:177]
	v_pk_mul_f32 v[208:209], v[118:119], v[186:187]
	v_pk_mul_f32 v[222:223], v[116:117], v[184:185]
	v_mad_i64_i32 v[206:207], s[34:35], v164, s36, v[176:177]
	v_lshl_or_b32 v178, s27, 9, v202
	v_mov_b32_e32 v179, v2
	v_and_b32_e32 v244, 3, v215
	v_lshrrev_b32_e32 v228, 4, v215
	v_sub_u32_e32 v228, v244, v228
	v_lshl_add_u32 v178, v228, 3, v178
	v_and_b32_e32 v228, 1, v215
	v_mad_u32_u24 v178, v228, 56, v178
	v_and_b32_e32 v228, 60, v215
	v_lshl_or_b32 v244, v244, 6, v228
	v_pk_fma_f32 v[208:209], v[126:127], v[198:199], v[208:209] neg_lo:[0,0,1] neg_hi:[0,0,1]
	v_pk_fma_f32 v[222:223], v[124:125], v[200:201], v[222:223] neg_lo:[0,0,1] neg_hi:[0,0,1]
	v_pk_mul_f32 v[224:225], v[126:127], v[186:187]
	v_pk_mul_f32 v[226:227], v[124:125], v[184:185]
	v_lshl_add_u64 v[206:207], v[206:207], 0, v[178:179]
	v_pk_fma_f32 v[224:225], v[118:119], v[198:199], v[224:225]
	v_pk_fma_f32 v[226:227], v[116:117], v[200:201], v[226:227]
	v_cvt_pk_bf16_f32 v222, v222, v223
	v_cvt_pk_bf16_f32 v223, v208, v209
	v_mad_i64_i32 v[192:193], s[34:35], v192, s36, v[176:177]
	v_cvt_pk_bf16_f32 v208, v226, v227
	v_cvt_pk_bf16_f32 v209, v224, v225
	v_mov_b32_e32 v228, v222
	v_mov_b32_e32 v229, v223
	v_mov_b32_e32 v230, v208
	v_mov_b32_e32 v231, v209
	s_nop 1
	v_permlane16_swap_b32_e32 v228, v230
	v_permlane16_swap_b32_e32 v229, v231
	ds_bpermute_b32 v228, v244, v228
	ds_bpermute_b32 v229, v244, v229
	ds_bpermute_b32 v230, v244, v230
	ds_bpermute_b32 v231, v244, v231
	v_pk_mul_f32 v[208:209], v[122:123], v[186:187]
	v_pk_mul_f32 v[222:223], v[120:121], v[184:185]
	v_pk_mul_f32 v[186:187], v[130:131], v[186:187]
	v_pk_mul_f32 v[184:185], v[128:129], v[184:185]
	v_pk_fma_f32 v[186:187], v[122:123], v[198:199], v[186:187]
	v_pk_fma_f32 v[184:185], v[120:121], v[200:201], v[184:185]
	v_pk_fma_f32 v[208:209], v[130:131], v[198:199], v[208:209] neg_lo:[0,0,1] neg_hi:[0,0,1]
	v_pk_fma_f32 v[222:223], v[128:129], v[200:201], v[222:223] neg_lo:[0,0,1] neg_hi:[0,0,1]
	v_lshl_add_u64 v[192:193], v[192:193], 0, v[178:179]
	v_cvt_pk_bf16_f32 v198, v222, v223
	v_cvt_pk_bf16_f32 v199, v208, v209
	v_cvt_pk_bf16_f32 v184, v184, v185
	v_cvt_pk_bf16_f32 v185, v186, v187
	v_pk_mul_f32 v[186:187], v[174:175], v[190:191] op_sel_hi:[0,1]
	v_pk_mul_f32 v[190:191], v[174:175], v[218:219] op_sel_hi:[0,1]
	v_mov_b32_e32 v232, v198
	v_mov_b32_e32 v233, v199
	v_mov_b32_e32 v234, v184
	v_mov_b32_e32 v235, v185
	s_nop 1
	v_permlane16_swap_b32_e32 v232, v234
	v_permlane16_swap_b32_e32 v233, v235
	ds_bpermute_b32 v232, v244, v232
	ds_bpermute_b32 v233, v244, v233
	ds_bpermute_b32 v234, v244, v234
	ds_bpermute_b32 v235, v244, v235
	s_waitcnt lgkmcnt(4)
; #define PG8_ST8(rs, b0, p, v) __builtin_amdgcn_raw_buffer_store_b64(v, rs, (int)((const char*)(p) - (const char*)(b0)), 0, 16)
; __device__ __forceinline__ unsigned cvt_pk_bf16(float lo, float hi) { unsigned r; asm volatile("v_cvt_pk_bf16_f32 %0, %1, %2" : "=v"(r) : "v"(lo), "v"(hi)); return r; }
;     __device__ __forceinline__ void operator()(const f32x4 (&acc)[2][2][4][2], const Unit& u, int wr, int wc, int fr, int fq) const {
;     ...
;                 for (int m = 0; m < 4; ++m) { const int row = row0 + ai * HALF + m * 16;
;                     const f32x4 cc = c4[m] * sc, ss = s4[m] * sc;
;                     bf16_t* rowp = P + (size_t)row * ldp + col0;
; #pragma unroll
;                     for (int bj = 0; bj < 2; ++bj) { const f32x4 x1 = acc[ai][bj][m][0], x2 = acc[ai][bj][m][1]; const f32x4 o1 = x1 * cc - x2 * ss, o2 = x2 * cc + x1 * ss;
;                         u32x2 w1, w2; w1.x = cvt_pk_bf16(o1[0], o1[1]); w1.y = cvt_pk_bf16(o1[2], o1[3]); w2.x = cvt_pk_bf16(o2[0], o2[1]); w2.y = cvt_pk_bf16(o2[2], o2[3]);
;                         PG8_ST8(rsp_, P, rowp + bj * HALF, w1); PG8_ST8(rsp_, P, rowp + bj * HALF + 32, w2); } }
	global_store_dwordx4 v[206:207], v[228:231], off
	v_pk_mul_f32 v[184:185], v[174:175], v[188:189] op_sel_hi:[0,1]
	v_pk_mul_f32 v[188:189], v[174:175], v[220:221] op_sel_hi:[0,1]
	v_pk_mul_f32 v[198:199], v[100:101], v[190:191]
	v_pk_mul_f32 v[200:201], v[102:103], v[188:189]
	v_pk_fma_f32 v[198:199], v[108:109], v[184:185], v[198:199] neg_lo:[0,0,1] neg_hi:[0,0,1]
	v_pk_fma_f32 v[200:201], v[110:111], v[186:187], v[200:201] neg_lo:[0,0,1] neg_hi:[0,0,1]
	v_pk_mul_f32 v[204:205], v[108:109], v[190:191]
	v_pk_mul_f32 v[208:209], v[110:111], v[188:189]
	v_cvt_pk_bf16_f32 v198, v198, v199
	v_cvt_pk_bf16_f32 v199, v200, v201
	v_pk_fma_f32 v[204:205], v[100:101], v[184:185], v[204:205]
	v_pk_fma_f32 v[208:209], v[102:103], v[186:187], v[208:209]
	v_cvt_pk_bf16_f32 v200, v204, v205
	v_pk_mul_f32 v[142:143], v[174:175], v[142:143] op_sel_hi:[0,1]
	v_cvt_pk_bf16_f32 v201, v208, v209
	v_mov_b32_e32 v236, v198
	v_mov_b32_e32 v237, v199
	v_mov_b32_e32 v238, v200
	v_mov_b32_e32 v239, v201
	s_nop 1
	v_permlane16_swap_b32_e32 v236, v238
	v_permlane16_swap_b32_e32 v237, v239
	ds_bpermute_b32 v236, v244, v236
	ds_bpermute_b32 v237, v244, v237
	ds_bpermute_b32 v238, v244, v238
	ds_bpermute_b32 v239, v244, v239
	s_waitcnt lgkmcnt(4)
	global_store_dwordx4 v[206:207], v[232:235], off offset:256
	v_pk_mul_f32 v[198:199], v[104:105], v[190:191]
	v_pk_mul_f32 v[190:191], v[112:113], v[190:191]
	v_pk_mul_f32 v[200:201], v[106:107], v[188:189]
	v_pk_fma_f32 v[198:199], v[112:113], v[184:185], v[198:199] neg_lo:[0,0,1] neg_hi:[0,0,1]
	v_pk_mul_f32 v[188:189], v[114:115], v[188:189]
	v_pk_fma_f32 v[184:185], v[104:105], v[184:185], v[190:191]
	v_pk_fma_f32 v[200:201], v[114:115], v[186:187], v[200:201] neg_lo:[0,0,1] neg_hi:[0,0,1]
	v_pk_fma_f32 v[186:187], v[106:107], v[186:187], v[188:189]
	v_cvt_pk_bf16_f32 v188, v198, v199
	v_cvt_pk_bf16_f32 v189, v200, v201
	v_cvt_pk_bf16_f32 v184, v184, v185
	v_pk_mul_f32 v[140:141], v[174:175], v[140:141] op_sel_hi:[0,1]
	v_cvt_pk_bf16_f32 v185, v186, v187
	v_mov_b32_e32 v240, v188
	v_mov_b32_e32 v241, v189
	v_mov_b32_e32 v242, v184
	v_mov_b32_e32 v243, v185
	s_nop 1
	v_permlane16_swap_b32_e32 v240, v242
	v_permlane16_swap_b32_e32 v241, v243
	ds_bpermute_b32 v240, v244, v240
	ds_bpermute_b32 v241, v244, v241
	ds_bpermute_b32 v242, v244, v242
	ds_bpermute_b32 v243, v244, v243
	s_waitcnt lgkmcnt(4)
	global_store_dwordx4 v[192:193], v[236:239], off
	v_pk_mul_f32 v[144:145], v[174:175], v[144:145] op_sel_hi:[0,1]
	v_pk_mul_f32 v[146:147], v[174:175], v[146:147] op_sel_hi:[0,1]
	v_pk_mul_f32 v[184:185], v[84:85], v[140:141]
	v_pk_mul_f32 v[186:187], v[86:87], v[142:143]
	v_mad_i64_i32 v[182:183], s[34:35], v182, s36, v[176:177]
	v_pk_fma_f32 v[186:187], v[94:95], v[146:147], v[186:187] neg_lo:[0,0,1] neg_hi:[0,0,1]
	v_pk_fma_f32 v[184:185], v[92:93], v[144:145], v[184:185] neg_lo:[0,0,1] neg_hi:[0,0,1]
	v_pk_mul_f32 v[188:189], v[92:93], v[140:141]
	v_pk_mul_f32 v[190:191], v[94:95], v[142:143]
	v_lshl_add_u64 v[182:183], v[182:183], 0, v[178:179]
	v_pk_fma_f32 v[190:191], v[86:87], v[146:147], v[190:191]
	v_pk_fma_f32 v[188:189], v[84:85], v[144:145], v[188:189]
	v_cvt_pk_bf16_f32 v184, v184, v185
	v_cvt_pk_bf16_f32 v185, v186, v187
	v_pk_mul_f32 v[134:135], v[174:175], v[134:135] op_sel_hi:[0,1]
	v_cvt_pk_bf16_f32 v186, v188, v189
	v_cvt_pk_bf16_f32 v187, v190, v191
	v_mov_b32_e32 v228, v184
	v_mov_b32_e32 v229, v185
	v_mov_b32_e32 v230, v186
	v_mov_b32_e32 v231, v187
	s_nop 1
	v_permlane16_swap_b32_e32 v228, v230
	v_permlane16_swap_b32_e32 v229, v231
	ds_bpermute_b32 v228, v244, v228
	ds_bpermute_b32 v229, v244, v229
	ds_bpermute_b32 v230, v244, v230
	ds_bpermute_b32 v231, v244, v231
	s_waitcnt lgkmcnt(4)
	global_store_dwordx4 v[192:193], v[240:243], off offset:256
	v_pk_mul_f32 v[184:185], v[88:89], v[140:141]
	v_pk_mul_f32 v[186:187], v[90:91], v[142:143]
	v_pk_mul_f32 v[140:141], v[96:97], v[140:141]
	v_pk_mul_f32 v[142:143], v[98:99], v[142:143]
	v_pk_fma_f32 v[186:187], v[98:99], v[146:147], v[186:187] neg_lo:[0,0,1] neg_hi:[0,0,1]
	v_pk_fma_f32 v[184:185], v[96:97], v[144:145], v[184:185] neg_lo:[0,0,1] neg_hi:[0,0,1]
	v_pk_fma_f32 v[142:143], v[90:91], v[146:147], v[142:143]
	v_pk_fma_f32 v[140:141], v[88:89], v[144:145], v[140:141]
	v_cvt_pk_bf16_f32 v144, v184, v185
	v_cvt_pk_bf16_f32 v145, v186, v187
	v_pk_mul_f32 v[132:133], v[174:175], v[132:133] op_sel_hi:[0,1]
	v_cvt_pk_bf16_f32 v140, v140, v141
	v_cvt_pk_bf16_f32 v141, v142, v143
	v_mov_b32_e32 v232, v144
	v_mov_b32_e32 v233, v145
	v_mov_b32_e32 v234, v140
	v_mov_b32_e32 v235, v141
	s_nop 1
	v_permlane16_swap_b32_e32 v232, v234
	v_permlane16_swap_b32_e32 v233, v235
	ds_bpermute_b32 v232, v244, v232
	ds_bpermute_b32 v233, v244, v233
	ds_bpermute_b32 v234, v244, v234
	ds_bpermute_b32 v235, v244, v235
	s_waitcnt lgkmcnt(4)
	global_store_dwordx4 v[182:183], v[228:231], off
	v_pk_mul_f32 v[136:137], v[174:175], v[136:137] op_sel_hi:[0,1]
	v_pk_mul_f32 v[138:139], v[174:175], v[138:139] op_sel_hi:[0,1]
	v_pk_mul_f32 v[142:143], v[68:69], v[132:133]
	v_pk_mul_f32 v[144:145], v[70:71], v[134:135]
	v_mad_i64_i32 v[140:141], s[34:35], v180, s36, v[176:177]
	v_pk_fma_f32 v[144:145], v[78:79], v[138:139], v[144:145] neg_lo:[0,0,1] neg_hi:[0,0,1]
	v_pk_fma_f32 v[142:143], v[76:77], v[136:137], v[142:143] neg_lo:[0,0,1] neg_hi:[0,0,1]
	v_pk_mul_f32 v[146:147], v[76:77], v[132:133]
	v_pk_mul_f32 v[180:181], v[78:79], v[134:135]
	v_lshl_add_u64 v[140:141], v[140:141], 0, v[178:179]
	v_pk_fma_f32 v[180:181], v[70:71], v[138:139], v[180:181]
	v_pk_fma_f32 v[146:147], v[68:69], v[136:137], v[146:147]
	v_cvt_pk_bf16_f32 v142, v142, v143
	v_cvt_pk_bf16_f32 v143, v144, v145
	v_lshlrev_b64 v[184:185], 7, v[168:169]
	v_cvt_pk_bf16_f32 v144, v146, v147
	v_cvt_pk_bf16_f32 v145, v180, v181
	v_mov_b32_e32 v236, v142
	v_mov_b32_e32 v237, v143
	v_mov_b32_e32 v238, v144
	v_mov_b32_e32 v239, v145
	s_nop 1
	v_permlane16_swap_b32_e32 v236, v238
	v_permlane16_swap_b32_e32 v237, v239
	ds_bpermute_b32 v236, v244, v236
	ds_bpermute_b32 v237, v244, v237
	ds_bpermute_b32 v238, v244, v238
	ds_bpermute_b32 v239, v244, v239
	s_waitcnt lgkmcnt(4)
; #define PG8_ST8(rs, b0, p, v) __builtin_amdgcn_raw_buffer_store_b64(v, rs, (int)((const char*)(p) - (const char*)(b0)), 0, 16)
; __device__ __forceinline__ unsigned cvt_pk_bf16(float lo, float hi) { unsigned r; asm volatile("v_cvt_pk_bf16_f32 %0, %1, %2" : "=v"(r) : "v"(lo), "v"(hi)); return r; }
;     __device__ __forceinline__ void operator()(const f32x4 (&acc)[2][2][4][2], const Unit& u, int wr, int wc, int fr, int fq) const {
;     ...
;             for (int ai = 0; ai < 2; ++ai) {
;                 f32x4 c4[4], s4[4];
; #pragma unroll
;                 for (int m = 0; m < 4; ++m) { const int row = row0 + ai * HALF + m * 16; c4[m] = *(const f32x4*)(rc + (size_t)row * 32 + f); s4[m] = *(const f32x4*)(rs + (size_t)row * 32 + f); }
;                 asm volatile("" ::: "memory");
; #pragma unroll
;                 for (int m = 0; m < 4; ++m) { const int row = row0 + ai * HALF + m * 16;
;                     const f32x4 cc = c4[m] * sc, ss = s4[m] * sc;
;                     bf16_t* rowp = P + (size_t)row * ldp + col0;
; #pragma unroll
;                     for (int bj = 0; bj < 2; ++bj) { const f32x4 x1 = acc[ai][bj][m][0], x2 = acc[ai][bj][m][1]; const f32x4 o1 = x1 * cc - x2 * ss, o2 = x2 * cc + x1 * ss;
;                         u32x2 w1, w2; w1.x = cvt_pk_bf16(o1[0], o1[1]); w1.y = cvt_pk_bf16(o1[2], o1[3]); w2.x = cvt_pk_bf16(o2[0], o2[1]); w2.y = cvt_pk_bf16(o2[2], o2[3]);
;                         PG8_ST8(rsp_, P, rowp + bj * HALF, w1); PG8_ST8(rsp_, P, rowp + bj * HALF + 32, w2); } }
	global_store_dwordx4 v[182:183], v[232:235], off offset:256
	v_pk_mul_f32 v[142:143], v[72:73], v[132:133]
	v_pk_mul_f32 v[144:145], v[74:75], v[134:135]
	v_pk_mul_f32 v[132:133], v[80:81], v[132:133]
	v_pk_fma_f32 v[144:145], v[82:83], v[138:139], v[144:145] neg_lo:[0,0,1] neg_hi:[0,0,1]
	v_pk_fma_f32 v[142:143], v[80:81], v[136:137], v[142:143] neg_lo:[0,0,1] neg_hi:[0,0,1]
	v_pk_mul_f32 v[134:135], v[82:83], v[134:135]
	v_pk_fma_f32 v[132:133], v[72:73], v[136:137], v[132:133]
	v_cvt_pk_bf16_f32 v136, v142, v143
	v_cvt_pk_bf16_f32 v137, v144, v145
	v_pk_fma_f32 v[134:135], v[74:75], v[138:139], v[134:135]
	v_cvt_pk_bf16_f32 v132, v132, v133
	v_lshlrev_b64 v[144:145], 7, v[170:171]
	v_cvt_pk_bf16_f32 v133, v134, v135
	v_mov_b32_e32 v240, v136
	v_mov_b32_e32 v241, v137
	v_mov_b32_e32 v242, v132
	v_mov_b32_e32 v243, v133
	s_nop 1
	v_permlane16_swap_b32_e32 v240, v242
	v_permlane16_swap_b32_e32 v241, v243
	ds_bpermute_b32 v240, v244, v240
	ds_bpermute_b32 v241, v244, v241
	ds_bpermute_b32 v242, v244, v242
	ds_bpermute_b32 v243, v244, v243
	s_waitcnt lgkmcnt(4)
	global_store_dwordx4 v[140:141], v[236:239], off
	s_waitcnt lgkmcnt(0)
	global_store_dwordx4 v[140:141], v[240:243], off offset:256
	v_lshlrev_b64 v[136:137], 7, v[172:173]
	v_lshl_add_u64 v[132:133], v[246:247], 0, v[136:137]
	v_lshl_add_u64 v[136:137], v[248:249], 0, v[136:137]
	global_load_dwordx4 v[132:135], v[132:133], off
	v_lshl_add_u64 v[140:141], v[246:247], 0, v[144:145]
	global_load_dwordx4 v[136:139], v[136:137], off
	v_lshl_add_u64 v[144:145], v[248:249], 0, v[144:145]
	global_load_dwordx4 v[140:143], v[140:141], off
	v_lshl_add_u64 v[180:181], v[246:247], 0, v[184:185]
	global_load_dwordx4 v[144:147], v[144:145], off
	v_lshl_add_u64 v[184:185], v[248:249], 0, v[184:185]
	global_load_dwordx4 v[180:183], v[180:181], off
	v_lshlrev_b64 v[192:193], 7, v[166:167]
	global_load_dwordx4 v[184:187], v[184:185], off
	v_lshl_add_u64 v[188:189], v[246:247], 0, v[192:193]
	v_lshl_add_u64 v[192:193], v[248:249], 0, v[192:193]
	global_load_dwordx4 v[188:191], v[188:189], off
	global_load_dwordx4 v[218:221], v[192:193], off
	s_waitcnt vmcnt(0)
	ds_bpermute_b32 v132, v245, v132
	ds_bpermute_b32 v133, v245, v133
	ds_bpermute_b32 v134, v245, v134
	ds_bpermute_b32 v135, v245, v135
	ds_bpermute_b32 v136, v245, v136
	ds_bpermute_b32 v137, v245, v137
	ds_bpermute_b32 v138, v245, v138
	ds_bpermute_b32 v139, v245, v139
	ds_bpermute_b32 v140, v245, v140
	ds_bpermute_b32 v141, v245, v141
	ds_bpermute_b32 v142, v245, v142
	ds_bpermute_b32 v143, v245, v143
	ds_bpermute_b32 v144, v245, v144
	ds_bpermute_b32 v145, v245, v145
	ds_bpermute_b32 v146, v245, v146
	ds_bpermute_b32 v147, v245, v147
	ds_bpermute_b32 v180, v245, v180
	ds_bpermute_b32 v181, v245, v181
	ds_bpermute_b32 v182, v245, v182
	ds_bpermute_b32 v183, v245, v183
	ds_bpermute_b32 v184, v245, v184
	ds_bpermute_b32 v185, v245, v185
	ds_bpermute_b32 v186, v245, v186
	ds_bpermute_b32 v187, v245, v187
	ds_bpermute_b32 v188, v245, v188
	ds_bpermute_b32 v189, v245, v189
	ds_bpermute_b32 v190, v245, v190
	ds_bpermute_b32 v191, v245, v191
	ds_bpermute_b32 v218, v245, v218
	ds_bpermute_b32 v219, v245, v219
	ds_bpermute_b32 v220, v245, v220
	ds_bpermute_b32 v221, v245, v221
	s_waitcnt lgkmcnt(0)
	v_pk_mul_f32 v[132:133], v[174:175], v[132:133] op_sel_hi:[0,1]
	v_pk_mul_f32 v[138:139], v[174:175], v[138:139] op_sel_hi:[0,1]
	v_pk_mul_f32 v[136:137], v[174:175], v[136:137] op_sel_hi:[0,1]
	v_pk_mul_f32 v[134:135], v[174:175], v[134:135] op_sel_hi:[0,1]
	v_pk_mul_f32 v[198:199], v[52:53], v[136:137]
	v_pk_mul_f32 v[200:201], v[54:55], v[138:139]
	v_mad_i64_i32 v[206:207], s[34:35], v172, s36, v[176:177]
	v_pk_fma_f32 v[200:201], v[62:63], v[134:135], v[200:201] neg_lo:[0,0,1] neg_hi:[0,0,1]
	v_pk_fma_f32 v[198:199], v[60:61], v[132:133], v[198:199] neg_lo:[0,0,1] neg_hi:[0,0,1]
	v_pk_mul_f32 v[204:205], v[60:61], v[136:137]
	v_pk_mul_f32 v[208:209], v[62:63], v[138:139]
	v_lshl_add_u64 v[206:207], v[206:207], 0, v[178:179]
	v_pk_fma_f32 v[208:209], v[54:55], v[134:135], v[208:209]
	v_pk_fma_f32 v[204:205], v[52:53], v[132:133], v[204:205]
	v_cvt_pk_bf16_f32 v198, v198, v199
	v_cvt_pk_bf16_f32 v199, v200, v201
	s_nop 0
	v_cvt_pk_bf16_f32 v200, v204, v205
	v_cvt_pk_bf16_f32 v201, v208, v209
	v_mov_b32_e32 v228, v198
	v_mov_b32_e32 v229, v199
	v_mov_b32_e32 v230, v200
	v_mov_b32_e32 v231, v201
	s_nop 1
	v_permlane16_swap_b32_e32 v228, v230
	v_permlane16_swap_b32_e32 v229, v231
	ds_bpermute_b32 v228, v244, v228
	ds_bpermute_b32 v229, v244, v229
	ds_bpermute_b32 v230, v244, v230
	ds_bpermute_b32 v231, v244, v231
	v_pk_mul_f32 v[198:199], v[56:57], v[136:137]
	v_pk_mul_f32 v[200:201], v[58:59], v[138:139]
	v_pk_mul_f32 v[136:137], v[64:65], v[136:137]
	v_pk_fma_f32 v[200:201], v[66:67], v[134:135], v[200:201] neg_lo:[0,0,1] neg_hi:[0,0,1]
	v_pk_fma_f32 v[198:199], v[64:65], v[132:133], v[198:199] neg_lo:[0,0,1] neg_hi:[0,0,1]
	v_pk_mul_f32 v[138:139], v[66:67], v[138:139]
	v_pk_fma_f32 v[132:133], v[56:57], v[132:133], v[136:137]
	v_cvt_pk_bf16_f32 v136, v198, v199
	v_cvt_pk_bf16_f32 v137, v200, v201
	v_pk_fma_f32 v[134:135], v[58:59], v[134:135], v[138:139]
	v_cvt_pk_bf16_f32 v132, v132, v133
	v_pk_mul_f32 v[138:139], v[174:175], v[144:145] op_sel_hi:[0,1]
	v_cvt_pk_bf16_f32 v133, v134, v135
	v_mov_b32_e32 v232, v136
	v_mov_b32_e32 v233, v137
	v_mov_b32_e32 v234, v132
	v_mov_b32_e32 v235, v133
	s_nop 1
	v_permlane16_swap_b32_e32 v232, v234
	v_permlane16_swap_b32_e32 v233, v235
	ds_bpermute_b32 v232, v244, v232
	ds_bpermute_b32 v233, v244, v233
	ds_bpermute_b32 v234, v244, v234
	ds_bpermute_b32 v235, v244, v235
	s_waitcnt lgkmcnt(4)
; #define PG8_ST8(rs, b0, p, v) __builtin_amdgcn_raw_buffer_store_b64(v, rs, (int)((const char*)(p) - (const char*)(b0)), 0, 16)
; __device__ __forceinline__ unsigned cvt_pk_bf16(float lo, float hi) { unsigned r; asm volatile("v_cvt_pk_bf16_f32 %0, %1, %2" : "=v"(r) : "v"(lo), "v"(hi)); return r; }
;     __device__ __forceinline__ void operator()(const f32x4 (&acc)[2][2][4][2], const Unit& u, int wr, int wc, int fr, int fq) const {
;     ...
;                 for (int m = 0; m < 4; ++m) { const int row = row0 + ai * HALF + m * 16;
;                     const f32x4 cc = c4[m] * sc, ss = s4[m] * sc;
;                     bf16_t* rowp = P + (size_t)row * ldp + col0;
; #pragma unroll
;                     for (int bj = 0; bj < 2; ++bj) { const f32x4 x1 = acc[ai][bj][m][0], x2 = acc[ai][bj][m][1]; const f32x4 o1 = x1 * cc - x2 * ss, o2 = x2 * cc + x1 * ss;
;                         u32x2 w1, w2; w1.x = cvt_pk_bf16(o1[0], o1[1]); w1.y = cvt_pk_bf16(o1[2], o1[3]); w2.x = cvt_pk_bf16(o2[0], o2[1]); w2.y = cvt_pk_bf16(o2[2], o2[3]);
;                         PG8_ST8(rsp_, P, rowp + bj * HALF, w1); PG8_ST8(rsp_, P, rowp + bj * HALF + 32, w2); } }
	global_store_dwordx4 v[206:207], v[228:231], off
	v_pk_mul_f32 v[136:137], v[174:175], v[146:147] op_sel_hi:[0,1]
	v_pk_mul_f32 v[132:133], v[174:175], v[140:141] op_sel_hi:[0,1]
	v_pk_mul_f32 v[134:135], v[174:175], v[142:143] op_sel_hi:[0,1]
	v_pk_mul_f32 v[142:143], v[36:37], v[138:139]
	v_pk_mul_f32 v[144:145], v[38:39], v[136:137]
	v_mad_i64_i32 v[140:141], s[34:35], v170, s36, v[176:177]
	v_pk_fma_f32 v[144:145], v[46:47], v[134:135], v[144:145] neg_lo:[0,0,1] neg_hi:[0,0,1]
	v_pk_fma_f32 v[142:143], v[44:45], v[132:133], v[142:143] neg_lo:[0,0,1] neg_hi:[0,0,1]
	v_pk_mul_f32 v[146:147], v[44:45], v[138:139]
	v_pk_mul_f32 v[192:193], v[46:47], v[136:137]
	v_lshl_add_u64 v[140:141], v[140:141], 0, v[178:179]
	v_pk_fma_f32 v[192:193], v[38:39], v[134:135], v[192:193]
	v_pk_fma_f32 v[146:147], v[36:37], v[132:133], v[146:147]
	v_cvt_pk_bf16_f32 v142, v142, v143
	v_cvt_pk_bf16_f32 v143, v144, v145
	s_nop 0
	v_cvt_pk_bf16_f32 v144, v146, v147
	v_cvt_pk_bf16_f32 v145, v192, v193
	v_mov_b32_e32 v236, v142
	v_mov_b32_e32 v237, v143
	v_mov_b32_e32 v238, v144
	v_mov_b32_e32 v239, v145
	s_nop 1
	v_permlane16_swap_b32_e32 v236, v238
	v_permlane16_swap_b32_e32 v237, v239
	ds_bpermute_b32 v236, v244, v236
	ds_bpermute_b32 v237, v244, v237
	ds_bpermute_b32 v238, v244, v238
	ds_bpermute_b32 v239, v244, v239
	s_waitcnt lgkmcnt(4)
	global_store_dwordx4 v[206:207], v[232:235], off offset:256
	v_pk_mul_f32 v[142:143], v[40:41], v[138:139]
	v_pk_mul_f32 v[144:145], v[42:43], v[136:137]
	v_pk_mul_f32 v[138:139], v[48:49], v[138:139]
	v_pk_mul_f32 v[136:137], v[50:51], v[136:137]
	v_pk_fma_f32 v[144:145], v[50:51], v[134:135], v[144:145] neg_lo:[0,0,1] neg_hi:[0,0,1]
	v_pk_fma_f32 v[142:143], v[48:49], v[132:133], v[142:143] neg_lo:[0,0,1] neg_hi:[0,0,1]
	v_pk_fma_f32 v[134:135], v[42:43], v[134:135], v[136:137]
	v_pk_fma_f32 v[132:133], v[40:41], v[132:133], v[138:139]
	v_cvt_pk_bf16_f32 v136, v142, v143
	v_cvt_pk_bf16_f32 v137, v144, v145
	v_pk_mul_f32 v[138:139], v[174:175], v[184:185] op_sel_hi:[0,1]
	v_cvt_pk_bf16_f32 v132, v132, v133
	v_cvt_pk_bf16_f32 v133, v134, v135
	v_mov_b32_e32 v240, v136
	v_mov_b32_e32 v241, v137
	v_mov_b32_e32 v242, v132
	v_mov_b32_e32 v243, v133
	s_nop 1
	v_permlane16_swap_b32_e32 v240, v242
	v_permlane16_swap_b32_e32 v241, v243
	ds_bpermute_b32 v240, v244, v240
	ds_bpermute_b32 v241, v244, v241
	ds_bpermute_b32 v242, v244, v242
	ds_bpermute_b32 v243, v244, v243
	s_waitcnt lgkmcnt(4)
	global_store_dwordx4 v[140:141], v[236:239], off
	v_pk_mul_f32 v[136:137], v[174:175], v[186:187] op_sel_hi:[0,1]
	v_pk_mul_f32 v[132:133], v[174:175], v[180:181] op_sel_hi:[0,1]
	v_pk_mul_f32 v[134:135], v[174:175], v[182:183] op_sel_hi:[0,1]
	v_pk_mul_f32 v[142:143], v[20:21], v[138:139]
	v_pk_mul_f32 v[144:145], v[22:23], v[136:137]
	v_mad_i64_i32 v[206:207], s[34:35], v168, s36, v[176:177]
	v_pk_fma_f32 v[144:145], v[30:31], v[134:135], v[144:145] neg_lo:[0,0,1] neg_hi:[0,0,1]
	v_pk_fma_f32 v[142:143], v[28:29], v[132:133], v[142:143] neg_lo:[0,0,1] neg_hi:[0,0,1]
	v_pk_mul_f32 v[146:147], v[28:29], v[138:139]
	v_pk_mul_f32 v[180:181], v[30:31], v[136:137]
	v_lshl_add_u64 v[206:207], v[206:207], 0, v[178:179]
	v_pk_fma_f32 v[180:181], v[22:23], v[134:135], v[180:181]
	v_pk_fma_f32 v[146:147], v[20:21], v[132:133], v[146:147]
	v_cvt_pk_bf16_f32 v142, v142, v143
	v_cvt_pk_bf16_f32 v143, v144, v145
	s_nop 0
	v_cvt_pk_bf16_f32 v144, v146, v147
	v_cvt_pk_bf16_f32 v145, v180, v181
	v_mov_b32_e32 v228, v142
	v_mov_b32_e32 v229, v143
	v_mov_b32_e32 v230, v144
	v_mov_b32_e32 v231, v145
	s_nop 1
	v_permlane16_swap_b32_e32 v228, v230
	v_permlane16_swap_b32_e32 v229, v231
	ds_bpermute_b32 v228, v244, v228
	ds_bpermute_b32 v229, v244, v229
	ds_bpermute_b32 v230, v244, v230
	ds_bpermute_b32 v231, v244, v231
	s_waitcnt lgkmcnt(4)
; #define PG8_ST8(rs, b0, p, v) __builtin_amdgcn_raw_buffer_store_b64(v, rs, (int)((const char*)(p) - (const char*)(b0)), 0, 16)
; __device__ __forceinline__ unsigned cvt_pk_bf16(float lo, float hi) { unsigned r; asm volatile("v_cvt_pk_bf16_f32 %0, %1, %2" : "=v"(r) : "v"(lo), "v"(hi)); return r; }
;     __device__ __forceinline__ void operator()(const f32x4 (&acc)[2][2][4][2], const Unit& u, int wr, int wc, int fr, int fq) const {
;     ...
;                 for (int m = 0; m < 4; ++m) { const int row = row0 + ai * HALF + m * 16;
;                     const f32x4 cc = c4[m] * sc, ss = s4[m] * sc;
;                     bf16_t* rowp = P + (size_t)row * ldp + col0;
; #pragma unroll
;                     for (int bj = 0; bj < 2; ++bj) { const f32x4 x1 = acc[ai][bj][m][0], x2 = acc[ai][bj][m][1]; const f32x4 o1 = x1 * cc - x2 * ss, o2 = x2 * cc + x1 * ss;
;                         u32x2 w1, w2; w1.x = cvt_pk_bf16(o1[0], o1[1]); w1.y = cvt_pk_bf16(o1[2], o1[3]); w2.x = cvt_pk_bf16(o2[0], o2[1]); w2.y = cvt_pk_bf16(o2[2], o2[3]);
;                         PG8_ST8(rsp_, P, rowp + bj * HALF, w1); PG8_ST8(rsp_, P, rowp + bj * HALF + 32, w2); } }
	global_store_dwordx4 v[140:141], v[240:243], off offset:256
	v_pk_mul_f32 v[142:143], v[24:25], v[138:139]
	v_pk_mul_f32 v[144:145], v[26:27], v[136:137]
	v_pk_mul_f32 v[138:139], v[32:33], v[138:139]
	v_pk_mul_f32 v[136:137], v[34:35], v[136:137]
	v_pk_fma_f32 v[144:145], v[34:35], v[134:135], v[144:145] neg_lo:[0,0,1] neg_hi:[0,0,1]
	v_pk_fma_f32 v[142:143], v[32:33], v[132:133], v[142:143] neg_lo:[0,0,1] neg_hi:[0,0,1]
	v_pk_fma_f32 v[134:135], v[26:27], v[134:135], v[136:137]
	v_pk_fma_f32 v[132:133], v[24:25], v[132:133], v[138:139]
	v_cvt_pk_bf16_f32 v136, v142, v143
	v_cvt_pk_bf16_f32 v137, v144, v145
	v_pk_mul_f32 v[138:139], v[174:175], v[218:219] op_sel_hi:[0,1]
	v_cvt_pk_bf16_f32 v132, v132, v133
	v_cvt_pk_bf16_f32 v133, v134, v135
	v_mov_b32_e32 v232, v136
	v_mov_b32_e32 v233, v137
	v_mov_b32_e32 v234, v132
	v_mov_b32_e32 v235, v133
	s_nop 1
	v_permlane16_swap_b32_e32 v232, v234
	v_permlane16_swap_b32_e32 v233, v235
	ds_bpermute_b32 v232, v244, v232
	ds_bpermute_b32 v233, v244, v233
	ds_bpermute_b32 v234, v244, v234
	ds_bpermute_b32 v235, v244, v235
	s_waitcnt lgkmcnt(4)
	global_store_dwordx4 v[206:207], v[228:231], off
	v_pk_mul_f32 v[136:137], v[174:175], v[220:221] op_sel_hi:[0,1]
	v_pk_mul_f32 v[132:133], v[174:175], v[188:189] op_sel_hi:[0,1]
	v_pk_mul_f32 v[134:135], v[174:175], v[190:191] op_sel_hi:[0,1]
	v_pk_mul_f32 v[142:143], v[4:5], v[138:139]
	v_pk_mul_f32 v[144:145], v[6:7], v[136:137]
	v_mad_i64_i32 v[140:141], s[34:35], v166, s36, v[176:177]
	v_pk_fma_f32 v[144:145], v[14:15], v[134:135], v[144:145] neg_lo:[0,0,1] neg_hi:[0,0,1]
	v_pk_fma_f32 v[142:143], v[12:13], v[132:133], v[142:143] neg_lo:[0,0,1] neg_hi:[0,0,1]
	v_pk_mul_f32 v[146:147], v[12:13], v[138:139]
	v_pk_mul_f32 v[176:177], v[14:15], v[136:137]
	v_lshl_add_u64 v[140:141], v[140:141], 0, v[178:179]
	v_pk_fma_f32 v[176:177], v[6:7], v[134:135], v[176:177]
	v_pk_fma_f32 v[146:147], v[4:5], v[132:133], v[146:147]
	v_cvt_pk_bf16_f32 v142, v142, v143
	v_cvt_pk_bf16_f32 v143, v144, v145
	s_mov_b64 s[34:35], 0
	v_cvt_pk_bf16_f32 v144, v146, v147
	v_cvt_pk_bf16_f32 v145, v176, v177
	v_mov_b32_e32 v236, v142
	v_mov_b32_e32 v237, v143
	v_mov_b32_e32 v238, v144
	v_mov_b32_e32 v239, v145
	s_nop 1
	v_permlane16_swap_b32_e32 v236, v238
	v_permlane16_swap_b32_e32 v237, v239
	ds_bpermute_b32 v236, v244, v236
	ds_bpermute_b32 v237, v244, v237
	ds_bpermute_b32 v238, v244, v238
	ds_bpermute_b32 v239, v244, v239
	s_waitcnt lgkmcnt(4)
	global_store_dwordx4 v[206:207], v[232:235], off offset:256
	v_pk_mul_f32 v[142:143], v[8:9], v[138:139]
	v_pk_mul_f32 v[144:145], v[10:11], v[136:137]
	v_pk_mul_f32 v[138:139], v[16:17], v[138:139]
	v_pk_mul_f32 v[136:137], v[18:19], v[136:137]
	v_pk_fma_f32 v[144:145], v[18:19], v[134:135], v[144:145] neg_lo:[0,0,1] neg_hi:[0,0,1]
	v_pk_fma_f32 v[142:143], v[16:17], v[132:133], v[142:143] neg_lo:[0,0,1] neg_hi:[0,0,1]
	v_pk_fma_f32 v[134:135], v[10:11], v[134:135], v[136:137]
	v_pk_fma_f32 v[132:133], v[8:9], v[132:133], v[138:139]
	v_cvt_pk_bf16_f32 v136, v142, v143
	v_cvt_pk_bf16_f32 v137, v144, v145
	s_nop 0
	v_cvt_pk_bf16_f32 v132, v132, v133
	v_cvt_pk_bf16_f32 v133, v134, v135
	v_mov_b32_e32 v240, v136
	v_mov_b32_e32 v241, v137
	v_mov_b32_e32 v242, v132
	v_mov_b32_e32 v243, v133
	s_nop 1
	v_permlane16_swap_b32_e32 v240, v242
	v_permlane16_swap_b32_e32 v241, v243
	ds_bpermute_b32 v240, v244, v240
	ds_bpermute_b32 v241, v244, v241
	ds_bpermute_b32 v242, v244, v242
	ds_bpermute_b32 v243, v244, v243
	s_waitcnt lgkmcnt(4)
	global_store_dwordx4 v[140:141], v[236:239], off
	s_waitcnt lgkmcnt(0)
	global_store_dwordx4 v[140:141], v[240:243], off offset:256
